# speedup vs baseline: 1.0078x; 1.0069x over previous
.Lu0_1:
	ds_read_b64_tr_b16 v[178:179], v206 offset:24576
	ds_read_b64_tr_b16 v[180:181], v206 offset:25600
	s_waitcnt lgkmcnt(9)
	v_mfma_f32_32x32x16_f16 v[98:113], v[82:85], v[154:157], v[34:49]
	v_add_f32_e32 v224, v66, v70
	v_add_f32_e32 v225, v67, v71
	v_add_f32_e32 v226, v68, v72
	v_add_f32_e32 v227, v69, v73
	v_cvt_pk_f16_f32 v158, v66, v67
	v_cvt_pk_f16_f32 v159, v68, v69
	ds_read_b64_tr_b16 v[174:175], v207 offset:24576
	ds_read_b64_tr_b16 v[176:177], v207 offset:25600
	s_waitcnt lgkmcnt(10)
	v_mfma_f32_32x32x16_f16 v[82:97], v[170:173], v[154:157], v[34:49]
	v_add_f32_e32 v224, v74, v224
	v_add_f32_e32 v225, v75, v225
	v_add_f32_e32 v226, v76, v226
	v_add_f32_e32 v227, v77, v227
	v_cvt_pk_f16_f32 v160, v70, v71
	v_cvt_pk_f16_f32 v161, v72, v73
	ds_read_b64_tr_b16 v[170:171], v206 offset:26624
	ds_read_b64_tr_b16 v[172:173], v206 offset:27648
	s_waitcnt lgkmcnt(11)
	v_mfma_f32_32x32x16_f16 v[98:113], v[166:169], v[146:149], v[98:113]
	v_add_f32_e32 v224, v78, v224
	v_add_f32_e32 v225, v79, v225
	v_add_f32_e32 v226, v80, v226
	v_add_f32_e32 v227, v81, v227
	v_cvt_pk_f16_f32 v150, v74, v75
	v_cvt_pk_f16_f32 v151, v76, v77
	ds_read_b64_tr_b16 v[74:75], v207 offset:26624
	ds_read_b64_tr_b16 v[76:77], v207 offset:27648
	s_waitcnt lgkmcnt(12)
	v_mfma_f32_32x32x16_f16 v[82:97], v[162:165], v[146:149], v[82:97]
	v_add_f32_e32 v224, v50, v224
	v_add_f32_e32 v225, v51, v225
	v_add_f32_e32 v226, v52, v226
	v_add_f32_e32 v227, v53, v227
	v_cvt_pk_f16_f32 v152, v78, v79
	v_cvt_pk_f16_f32 v153, v80, v81
	ds_read_b64_tr_b16 v[70:71], v206 offset:28672
	ds_read_b64_tr_b16 v[72:73], v206 offset:29696
	s_waitcnt lgkmcnt(13)
	v_mfma_f32_32x32x16_f16 v[98:113], v[126:129], v[138:141], v[98:113]
	v_add_f32_e32 v224, v54, v224
	v_add_f32_e32 v225, v55, v225
	v_add_f32_e32 v226, v56, v226
	v_add_f32_e32 v227, v57, v227
	v_cvt_pk_f16_f32 v142, v50, v51
	v_cvt_pk_f16_f32 v143, v52, v53
	ds_read_b64_tr_b16 v[66:67], v207 offset:28672
	ds_read_b64_tr_b16 v[68:69], v207 offset:29696
	s_waitcnt lgkmcnt(14)
	v_mfma_f32_32x32x16_f16 v[82:97], v[122:125], v[138:141], v[82:97]
	v_add_f32_e32 v224, v58, v224
	v_add_f32_e32 v225, v59, v225
	v_add_f32_e32 v226, v60, v226
	v_add_f32_e32 v227, v61, v227
	v_cvt_pk_f16_f32 v144, v54, v55
	v_cvt_pk_f16_f32 v145, v56, v57
	ds_read_b64_tr_b16 v[54:55], v206 offset:30720
	ds_read_b64_tr_b16 v[56:57], v206 offset:31744
	s_waitcnt lgkmcnt(14)
	v_mfma_f32_32x32x16_f16 v[98:113], v[118:121], v[134:137], v[98:113]
	v_add_f32_e32 v224, v62, v224
	v_add_f32_e32 v225, v63, v225
	v_add_f32_e32 v226, v64, v226
	v_add_f32_e32 v227, v65, v227
	v_cvt_pk_f16_f32 v130, v58, v59
	v_cvt_pk_f16_f32 v131, v60, v61
	ds_read_b64_tr_b16 v[50:51], v207 offset:30720
	ds_read_b64_tr_b16 v[52:53], v207 offset:31744
	v_mfma_f32_32x32x16_f16 v[82:97], v[114:117], v[134:137], v[82:97]
	v_add_f32_e32 v224, v224, v225
	v_add_f32_e32 v226, v226, v227
	v_add_f32_e32 v60, v224, v226
	v_cvt_pk_f16_f32 v132, v62, v63
	v_cvt_pk_f16_f32 v133, v64, v65
	s_add_i32 s26, s42, s36
	s_mov_b32 m0, s26
	s_nop 0
	global_load_lds_dwordx4 v221, s[50:51]
	s_add_i32 s26, s39, s35
	s_mov_b32 m0, s26
	s_nop 0
	global_load_lds_dwordx4 v222, s[52:53]
	v_max_f32_e32 v58, v98, v99
	v_max3_f32 v59, v100, v101, v83
	v_max3_f32 v58, v58, v82, v84
	v_max3_f32 v58, v58, v85, v102
	v_max3_f32 v59, v59, v104, v105
	v_max3_f32 v58, v58, v103, v86
	v_max3_f32 v59, v59, v88, v89
	v_max3_f32 v58, v58, v87, v106
	v_max3_f32 v59, v59, v108, v109
	v_max3_f32 v58, v58, v107, v90
	v_max3_f32 v59, v59, v92, v93
	v_max3_f32 v58, v58, v91, v110
	v_max3_f32 v59, v59, v112, v113
	v_max3_f32 v58, v58, v111, v94
	v_max3_f32 v59, v59, v96, v97
	v_max3_f32 v58, v58, v95, v59
	v_add_f32_e32 v198, v183, v60
	v_cmp_lt_f32_e32 vcc, s41, v58
	s_cmp_lg_u64 vcc, 0
	s_cselect_b64 s[26:27], -1, 0
	s_cbranch_vccnz .Lu0_9

.Lu0_4:
	s_add_i32 s26, s39, 0x2000
	s_cmpk_lg_i32 s39, 0x4000
	s_cselect_b32 s43, s26, 0
	ds_read_b64_tr_b16 v[126:127], v206 offset:32768
	ds_read_b64_tr_b16 v[128:129], v206 offset:33792
	s_waitcnt lgkmcnt(9)
	v_mfma_f32_32x32x16_f16 v[66:81], v[58:61], v[154:157], v[34:49]
	v_add_f32_e32 v224, v98, v102
	v_add_f32_e32 v225, v99, v103
	v_add_f32_e32 v226, v100, v104
	v_add_f32_e32 v227, v101, v105
	v_cvt_pk_f16_f32 v158, v98, v99
	v_cvt_pk_f16_f32 v159, v100, v101
	ds_read_b64_tr_b16 v[122:123], v207 offset:32768
	ds_read_b64_tr_b16 v[124:125], v207 offset:33792
	s_waitcnt lgkmcnt(10)
	v_mfma_f32_32x32x16_f16 v[50:65], v[114:117], v[154:157], v[34:49]
	v_add_f32_e32 v224, v106, v224
	v_add_f32_e32 v225, v107, v225
	v_add_f32_e32 v226, v108, v226
	v_add_f32_e32 v227, v109, v227
	v_cvt_pk_f16_f32 v160, v102, v103
	v_cvt_pk_f16_f32 v161, v104, v105
	ds_read_b64_tr_b16 v[118:119], v206 offset:34816
	ds_read_b64_tr_b16 v[120:121], v206 offset:35840
	s_waitcnt lgkmcnt(11)
	v_mfma_f32_32x32x16_f16 v[66:81], v[182:185], v[146:149], v[66:81]
	v_add_f32_e32 v224, v110, v224
	v_add_f32_e32 v225, v111, v225
	v_add_f32_e32 v226, v112, v226
	v_add_f32_e32 v227, v113, v227
	v_cvt_pk_f16_f32 v150, v106, v107
	v_cvt_pk_f16_f32 v151, v108, v109
	ds_read_b64_tr_b16 v[114:115], v207 offset:34816
	ds_read_b64_tr_b16 v[116:117], v207 offset:35840
	s_waitcnt lgkmcnt(12)
	v_mfma_f32_32x32x16_f16 v[50:65], v[174:177], v[146:149], v[50:65]
	v_add_f32_e32 v224, v82, v224
	v_add_f32_e32 v225, v83, v225
	v_add_f32_e32 v226, v84, v226
	v_add_f32_e32 v227, v85, v227
	v_cvt_pk_f16_f32 v152, v110, v111
	v_cvt_pk_f16_f32 v153, v112, v113
	ds_read_b64_tr_b16 v[106:107], v206 offset:36864
	ds_read_b64_tr_b16 v[108:109], v206 offset:37888
	s_waitcnt lgkmcnt(13)
	v_mfma_f32_32x32x16_f16 v[66:81], v[178:181], v[138:141], v[66:81]
	v_add_f32_e32 v224, v86, v224
	v_add_f32_e32 v225, v87, v225
	v_add_f32_e32 v226, v88, v226
	v_add_f32_e32 v227, v89, v227
	v_cvt_pk_f16_f32 v142, v82, v83
	v_cvt_pk_f16_f32 v143, v84, v85
	ds_read_b64_tr_b16 v[102:103], v207 offset:36864
	ds_read_b64_tr_b16 v[104:105], v207 offset:37888
	s_waitcnt lgkmcnt(14)
	v_mfma_f32_32x32x16_f16 v[50:65], v[166:169], v[138:141], v[50:65]
	v_add_f32_e32 v224, v90, v224
	v_add_f32_e32 v225, v91, v225
	v_add_f32_e32 v226, v92, v226
	v_add_f32_e32 v227, v93, v227
	v_cvt_pk_f16_f32 v144, v86, v87
	v_cvt_pk_f16_f32 v145, v88, v89
	ds_read_b64_tr_b16 v[98:99], v206 offset:38912
	ds_read_b64_tr_b16 v[100:101], v206 offset:39936
	s_waitcnt lgkmcnt(14)
	v_mfma_f32_32x32x16_f16 v[66:81], v[170:173], v[134:137], v[66:81]
	v_add_f32_e32 v224, v94, v224
	v_add_f32_e32 v225, v95, v225
	v_add_f32_e32 v226, v96, v226
	v_add_f32_e32 v227, v97, v227
	v_cvt_pk_f16_f32 v130, v90, v91
	v_cvt_pk_f16_f32 v131, v92, v93
	ds_read_b64_tr_b16 v[86:87], v207 offset:38912
	ds_read_b64_tr_b16 v[88:89], v207 offset:39936
	v_mfma_f32_32x32x16_f16 v[50:65], v[162:165], v[134:137], v[50:65]
	v_add_f32_e32 v224, v224, v225
	v_add_f32_e32 v226, v226, v227
	v_add_f32_e32 v84, v224, v226
	v_cvt_pk_f16_f32 v132, v94, v95
	v_cvt_pk_f16_f32 v133, v96, v97
	s_add_u32 s54, s50, 0x2000
	s_addc_u32 s55, s51, 0
	s_add_i32 s26, s39, s36
	s_mov_b32 m0, s26
	s_nop 0
	global_load_lds_dwordx4 v221, s[54:55]
	v_max_f32_e32 v82, v66, v67
	s_nop 1
	v_max3_f32 v83, v68, v69, v51
	v_max3_f32 v82, v82, v50, v52
	v_max3_f32 v82, v82, v53, v70
	v_max3_f32 v83, v83, v72, v73
	v_max3_f32 v82, v82, v71, v54
	v_max3_f32 v83, v83, v56, v57
	v_max3_f32 v82, v82, v55, v74
	v_max3_f32 v83, v83, v76, v77
	v_max3_f32 v82, v82, v75, v58
	v_max3_f32 v83, v83, v60, v61
	v_max3_f32 v82, v82, v59, v78
	v_max3_f32 v83, v83, v80, v81
	v_max3_f32 v82, v82, v79, v62
	v_max3_f32 v83, v83, v64, v65
	v_max3_f32 v82, v82, v63, v83
	v_add_f32_e32 v183, v198, v84
	s_add_u32 s54, s52, 0x2000
	s_addc_u32 s55, s53, 0
	s_add_i32 s26, s43, s35
	s_mov_b32 m0, s26
	s_nop 0
	global_load_lds_dwordx4 v222, s[54:55]
	v_cmp_lt_f32_e32 vcc, s41, v82
	s_cmp_lg_u64 vcc, 0
	s_cselect_b64 s[26:27], -1, 0
	s_cbranch_vccnz .Lu0_12

.Lu1_1:
	ds_read_b64_tr_b16 v[178:179], v206 offset:40960
	ds_read_b64_tr_b16 v[180:181], v206 offset:41984
	s_waitcnt lgkmcnt(9)
	v_mfma_f32_32x32x16_f16 v[98:113], v[82:85], v[154:157], v[34:49]
	v_add_f32_e32 v224, v66, v70
	v_add_f32_e32 v225, v67, v71
	v_add_f32_e32 v226, v68, v72
	v_add_f32_e32 v227, v69, v73
	v_cvt_pk_f16_f32 v158, v66, v67
	v_cvt_pk_f16_f32 v159, v68, v69
	ds_read_b64_tr_b16 v[174:175], v207 offset:40960
	ds_read_b64_tr_b16 v[176:177], v207 offset:41984
	s_waitcnt lgkmcnt(10)
	v_mfma_f32_32x32x16_f16 v[82:97], v[170:173], v[154:157], v[34:49]
	v_add_f32_e32 v224, v74, v224
	v_add_f32_e32 v225, v75, v225
	v_add_f32_e32 v226, v76, v226
	v_add_f32_e32 v227, v77, v227
	v_cvt_pk_f16_f32 v160, v70, v71
	v_cvt_pk_f16_f32 v161, v72, v73
	ds_read_b64_tr_b16 v[170:171], v206 offset:43008
	ds_read_b64_tr_b16 v[172:173], v206 offset:44032
	s_waitcnt lgkmcnt(11)
	v_mfma_f32_32x32x16_f16 v[98:113], v[166:169], v[146:149], v[98:113]
	v_add_f32_e32 v224, v78, v224
	v_add_f32_e32 v225, v79, v225
	v_add_f32_e32 v226, v80, v226
	v_add_f32_e32 v227, v81, v227
	v_cvt_pk_f16_f32 v150, v74, v75
	v_cvt_pk_f16_f32 v151, v76, v77
	ds_read_b64_tr_b16 v[74:75], v207 offset:43008
	ds_read_b64_tr_b16 v[76:77], v207 offset:44032
	s_waitcnt lgkmcnt(12)
	v_mfma_f32_32x32x16_f16 v[82:97], v[162:165], v[146:149], v[82:97]
	v_add_f32_e32 v224, v50, v224
	v_add_f32_e32 v225, v51, v225
	v_add_f32_e32 v226, v52, v226
	v_add_f32_e32 v227, v53, v227
	v_cvt_pk_f16_f32 v152, v78, v79
	v_cvt_pk_f16_f32 v153, v80, v81
	ds_read_b64_tr_b16 v[70:71], v206 offset:45056
	ds_read_b64_tr_b16 v[72:73], v206 offset:46080
	s_waitcnt lgkmcnt(13)
	v_mfma_f32_32x32x16_f16 v[98:113], v[126:129], v[138:141], v[98:113]
	v_add_f32_e32 v224, v54, v224
	v_add_f32_e32 v225, v55, v225
	v_add_f32_e32 v226, v56, v226
	v_add_f32_e32 v227, v57, v227
	v_cvt_pk_f16_f32 v142, v50, v51
	v_cvt_pk_f16_f32 v143, v52, v53
	ds_read_b64_tr_b16 v[66:67], v207 offset:45056
	ds_read_b64_tr_b16 v[68:69], v207 offset:46080
	s_waitcnt lgkmcnt(14)
	v_mfma_f32_32x32x16_f16 v[82:97], v[122:125], v[138:141], v[82:97]
	v_add_f32_e32 v224, v58, v224
	v_add_f32_e32 v225, v59, v225
	v_add_f32_e32 v226, v60, v226
	v_add_f32_e32 v227, v61, v227
	v_cvt_pk_f16_f32 v144, v54, v55
	v_cvt_pk_f16_f32 v145, v56, v57
	ds_read_b64_tr_b16 v[54:55], v206 offset:47104
	ds_read_b64_tr_b16 v[56:57], v206 offset:48128
	s_waitcnt lgkmcnt(14)
	v_mfma_f32_32x32x16_f16 v[98:113], v[118:121], v[134:137], v[98:113]
	v_add_f32_e32 v224, v62, v224
	v_add_f32_e32 v225, v63, v225
	v_add_f32_e32 v226, v64, v226
	v_add_f32_e32 v227, v65, v227
	v_cvt_pk_f16_f32 v130, v58, v59
	v_cvt_pk_f16_f32 v131, v60, v61
	ds_read_b64_tr_b16 v[50:51], v207 offset:47104
	ds_read_b64_tr_b16 v[52:53], v207 offset:48128
	v_mfma_f32_32x32x16_f16 v[82:97], v[114:117], v[134:137], v[82:97]
	v_add_f32_e32 v224, v224, v225
	v_add_f32_e32 v226, v226, v227
	v_add_f32_e32 v60, v224, v226
	v_cvt_pk_f16_f32 v132, v62, v63
	v_cvt_pk_f16_f32 v133, v64, v65
	s_add_i32 s26, s42, s36
	s_mov_b32 m0, s26
	s_nop 0
	global_load_lds_dwordx4 v221, s[50:51]
	s_add_i32 s26, s39, s35
	s_mov_b32 m0, s26
	s_nop 0
	global_load_lds_dwordx4 v222, s[52:53]
	v_max_f32_e32 v58, v98, v99
	v_max3_f32 v59, v100, v101, v83
	v_max3_f32 v58, v58, v82, v84
	v_max3_f32 v58, v58, v85, v102
	v_max3_f32 v59, v59, v104, v105
	v_max3_f32 v58, v58, v103, v86
	v_max3_f32 v59, v59, v88, v89
	v_max3_f32 v58, v58, v87, v106
	v_max3_f32 v59, v59, v108, v109
	v_max3_f32 v58, v58, v107, v90
	v_max3_f32 v59, v59, v92, v93
	v_max3_f32 v58, v58, v91, v110
	v_max3_f32 v59, v59, v112, v113
	v_max3_f32 v58, v58, v111, v94
	v_max3_f32 v59, v59, v96, v97
	v_max3_f32 v58, v58, v95, v59
	v_add_f32_e32 v198, v183, v60
	v_cmp_lt_f32_e32 vcc, s41, v58
	s_cmp_lg_u64 vcc, 0
	s_cselect_b64 s[26:27], -1, 0
	s_cbranch_vccnz .Lu1_9

.Lu1_4:
	s_add_i32 s26, s39, 0x2000
	s_cmpk_lg_i32 s39, 0x4000
	s_cselect_b32 s43, s26, 0
	ds_read_b64_tr_b16 v[126:127], v206 offset:24576
	ds_read_b64_tr_b16 v[128:129], v206 offset:25600
	s_waitcnt lgkmcnt(9)
	v_mfma_f32_32x32x16_f16 v[66:81], v[58:61], v[154:157], v[34:49]
	v_add_f32_e32 v224, v98, v102
	v_add_f32_e32 v225, v99, v103
	v_add_f32_e32 v226, v100, v104
	v_add_f32_e32 v227, v101, v105
	v_cvt_pk_f16_f32 v158, v98, v99
	v_cvt_pk_f16_f32 v159, v100, v101
	ds_read_b64_tr_b16 v[122:123], v207 offset:24576
	ds_read_b64_tr_b16 v[124:125], v207 offset:25600
	s_waitcnt lgkmcnt(10)
	v_mfma_f32_32x32x16_f16 v[50:65], v[114:117], v[154:157], v[34:49]
	v_add_f32_e32 v224, v106, v224
	v_add_f32_e32 v225, v107, v225
	v_add_f32_e32 v226, v108, v226
	v_add_f32_e32 v227, v109, v227
	v_cvt_pk_f16_f32 v160, v102, v103
	v_cvt_pk_f16_f32 v161, v104, v105
	ds_read_b64_tr_b16 v[118:119], v206 offset:26624
	ds_read_b64_tr_b16 v[120:121], v206 offset:27648
	s_waitcnt lgkmcnt(11)
	v_mfma_f32_32x32x16_f16 v[66:81], v[182:185], v[146:149], v[66:81]
	v_add_f32_e32 v224, v110, v224
	v_add_f32_e32 v225, v111, v225
	v_add_f32_e32 v226, v112, v226
	v_add_f32_e32 v227, v113, v227
	v_cvt_pk_f16_f32 v150, v106, v107
	v_cvt_pk_f16_f32 v151, v108, v109
	ds_read_b64_tr_b16 v[114:115], v207 offset:26624
	ds_read_b64_tr_b16 v[116:117], v207 offset:27648
	s_waitcnt lgkmcnt(12)
	v_mfma_f32_32x32x16_f16 v[50:65], v[174:177], v[146:149], v[50:65]
	v_add_f32_e32 v224, v82, v224
	v_add_f32_e32 v225, v83, v225
	v_add_f32_e32 v226, v84, v226
	v_add_f32_e32 v227, v85, v227
	v_cvt_pk_f16_f32 v152, v110, v111
	v_cvt_pk_f16_f32 v153, v112, v113
	ds_read_b64_tr_b16 v[106:107], v206 offset:28672
	ds_read_b64_tr_b16 v[108:109], v206 offset:29696
	s_waitcnt lgkmcnt(13)
	v_mfma_f32_32x32x16_f16 v[66:81], v[178:181], v[138:141], v[66:81]
	v_add_f32_e32 v224, v86, v224
	v_add_f32_e32 v225, v87, v225
	v_add_f32_e32 v226, v88, v226
	v_add_f32_e32 v227, v89, v227
	v_cvt_pk_f16_f32 v142, v82, v83
	v_cvt_pk_f16_f32 v143, v84, v85
	ds_read_b64_tr_b16 v[102:103], v207 offset:28672
	ds_read_b64_tr_b16 v[104:105], v207 offset:29696
	s_waitcnt lgkmcnt(14)
	v_mfma_f32_32x32x16_f16 v[50:65], v[166:169], v[138:141], v[50:65]
	v_add_f32_e32 v224, v90, v224
	v_add_f32_e32 v225, v91, v225
	v_add_f32_e32 v226, v92, v226
	v_add_f32_e32 v227, v93, v227
	v_cvt_pk_f16_f32 v144, v86, v87
	v_cvt_pk_f16_f32 v145, v88, v89
	ds_read_b64_tr_b16 v[98:99], v206 offset:30720
	ds_read_b64_tr_b16 v[100:101], v206 offset:31744
	s_waitcnt lgkmcnt(14)
	v_mfma_f32_32x32x16_f16 v[66:81], v[170:173], v[134:137], v[66:81]
	v_add_f32_e32 v224, v94, v224
	v_add_f32_e32 v225, v95, v225
	v_add_f32_e32 v226, v96, v226
	v_add_f32_e32 v227, v97, v227
	v_cvt_pk_f16_f32 v130, v90, v91
	v_cvt_pk_f16_f32 v131, v92, v93
	ds_read_b64_tr_b16 v[86:87], v207 offset:30720
	ds_read_b64_tr_b16 v[88:89], v207 offset:31744
	v_mfma_f32_32x32x16_f16 v[50:65], v[162:165], v[134:137], v[50:65]
	v_add_f32_e32 v224, v224, v225
	v_add_f32_e32 v226, v226, v227
	v_add_f32_e32 v84, v224, v226
	v_cvt_pk_f16_f32 v132, v94, v95
	v_cvt_pk_f16_f32 v133, v96, v97
	s_add_u32 s54, s50, 0x2000
	s_addc_u32 s55, s51, 0
	s_add_i32 s26, s39, s36
	s_mov_b32 m0, s26
	s_nop 0
	global_load_lds_dwordx4 v221, s[54:55]
	v_max_f32_e32 v82, v66, v67
	s_nop 1
	v_max3_f32 v83, v68, v69, v51
	v_max3_f32 v82, v82, v50, v52
	v_max3_f32 v82, v82, v53, v70
	v_max3_f32 v83, v83, v72, v73
	v_max3_f32 v82, v82, v71, v54
	v_max3_f32 v83, v83, v56, v57
	v_max3_f32 v82, v82, v55, v74
	v_max3_f32 v83, v83, v76, v77
	v_max3_f32 v82, v82, v75, v58
	v_max3_f32 v83, v83, v60, v61
	v_max3_f32 v82, v82, v59, v78
	v_max3_f32 v83, v83, v80, v81
	v_max3_f32 v82, v82, v79, v62
	v_max3_f32 v83, v83, v64, v65
	v_max3_f32 v82, v82, v63, v83
	v_add_f32_e32 v183, v198, v84
	s_add_u32 s54, s52, 0x2000
	s_addc_u32 s55, s53, 0
	s_add_i32 s26, s43, s35
	s_mov_b32 m0, s26
	s_nop 0
	global_load_lds_dwordx4 v222, s[54:55]
	v_cmp_lt_f32_e32 vcc, s41, v82
	s_cmp_lg_u64 vcc, 0
	s_cselect_b64 s[26:27], -1, 0
	s_cbranch_vccnz .Lu1_12

.Lu2_1:
	ds_read_b64_tr_b16 v[178:179], v206 offset:32768
	ds_read_b64_tr_b16 v[180:181], v206 offset:33792
	s_waitcnt lgkmcnt(9)
	v_mfma_f32_32x32x16_f16 v[98:113], v[82:85], v[154:157], v[34:49]
	v_add_f32_e32 v224, v66, v70
	v_add_f32_e32 v225, v67, v71
	v_add_f32_e32 v226, v68, v72
	v_add_f32_e32 v227, v69, v73
	v_cvt_pk_f16_f32 v158, v66, v67
	v_cvt_pk_f16_f32 v159, v68, v69
	ds_read_b64_tr_b16 v[174:175], v207 offset:32768
	ds_read_b64_tr_b16 v[176:177], v207 offset:33792
	s_waitcnt lgkmcnt(10)
	v_mfma_f32_32x32x16_f16 v[82:97], v[170:173], v[154:157], v[34:49]
	v_add_f32_e32 v224, v74, v224
	v_add_f32_e32 v225, v75, v225
	v_add_f32_e32 v226, v76, v226
	v_add_f32_e32 v227, v77, v227
	v_cvt_pk_f16_f32 v160, v70, v71
	v_cvt_pk_f16_f32 v161, v72, v73
	ds_read_b64_tr_b16 v[170:171], v206 offset:34816
	ds_read_b64_tr_b16 v[172:173], v206 offset:35840
	s_waitcnt lgkmcnt(11)
	v_mfma_f32_32x32x16_f16 v[98:113], v[166:169], v[146:149], v[98:113]
	v_add_f32_e32 v224, v78, v224
	v_add_f32_e32 v225, v79, v225
	v_add_f32_e32 v226, v80, v226
	v_add_f32_e32 v227, v81, v227
	v_cvt_pk_f16_f32 v150, v74, v75
	v_cvt_pk_f16_f32 v151, v76, v77
	ds_read_b64_tr_b16 v[74:75], v207 offset:34816
	ds_read_b64_tr_b16 v[76:77], v207 offset:35840
	s_waitcnt lgkmcnt(12)
	v_mfma_f32_32x32x16_f16 v[82:97], v[162:165], v[146:149], v[82:97]
	v_add_f32_e32 v224, v50, v224
	v_add_f32_e32 v225, v51, v225
	v_add_f32_e32 v226, v52, v226
	v_add_f32_e32 v227, v53, v227
	v_cvt_pk_f16_f32 v152, v78, v79
	v_cvt_pk_f16_f32 v153, v80, v81
	ds_read_b64_tr_b16 v[70:71], v206 offset:36864
	ds_read_b64_tr_b16 v[72:73], v206 offset:37888
	s_waitcnt lgkmcnt(13)
	v_mfma_f32_32x32x16_f16 v[98:113], v[126:129], v[138:141], v[98:113]
	v_add_f32_e32 v224, v54, v224
	v_add_f32_e32 v225, v55, v225
	v_add_f32_e32 v226, v56, v226
	v_add_f32_e32 v227, v57, v227
	v_cvt_pk_f16_f32 v142, v50, v51
	v_cvt_pk_f16_f32 v143, v52, v53
	ds_read_b64_tr_b16 v[66:67], v207 offset:36864
	ds_read_b64_tr_b16 v[68:69], v207 offset:37888
	s_waitcnt lgkmcnt(14)
	v_mfma_f32_32x32x16_f16 v[82:97], v[122:125], v[138:141], v[82:97]
	v_add_f32_e32 v224, v58, v224
	v_add_f32_e32 v225, v59, v225
	v_add_f32_e32 v226, v60, v226
	v_add_f32_e32 v227, v61, v227
	v_cvt_pk_f16_f32 v144, v54, v55
	v_cvt_pk_f16_f32 v145, v56, v57
	ds_read_b64_tr_b16 v[54:55], v206 offset:38912
	ds_read_b64_tr_b16 v[56:57], v206 offset:39936
	s_waitcnt lgkmcnt(14)
	v_mfma_f32_32x32x16_f16 v[98:113], v[118:121], v[134:137], v[98:113]
	v_add_f32_e32 v224, v62, v224
	v_add_f32_e32 v225, v63, v225
	v_add_f32_e32 v226, v64, v226
	v_add_f32_e32 v227, v65, v227
	v_cvt_pk_f16_f32 v130, v58, v59
	v_cvt_pk_f16_f32 v131, v60, v61
	ds_read_b64_tr_b16 v[50:51], v207 offset:38912
	ds_read_b64_tr_b16 v[52:53], v207 offset:39936
	v_mfma_f32_32x32x16_f16 v[82:97], v[114:117], v[134:137], v[82:97]
	v_add_f32_e32 v224, v224, v225
	v_add_f32_e32 v226, v226, v227
	v_add_f32_e32 v60, v224, v226
	v_cvt_pk_f16_f32 v132, v62, v63
	v_cvt_pk_f16_f32 v133, v64, v65
	s_add_i32 s26, s42, s36
	s_mov_b32 m0, s26
	s_nop 0
	global_load_lds_dwordx4 v221, s[50:51]
	s_add_i32 s26, s39, s35
	s_mov_b32 m0, s26
	s_nop 0
	global_load_lds_dwordx4 v222, s[52:53]
	v_max_f32_e32 v58, v98, v99
	v_max3_f32 v59, v100, v101, v83
	v_max3_f32 v58, v58, v82, v84
	v_max3_f32 v58, v58, v85, v102
	v_max3_f32 v59, v59, v104, v105
	v_max3_f32 v58, v58, v103, v86
	v_max3_f32 v59, v59, v88, v89
	v_max3_f32 v58, v58, v87, v106
	v_max3_f32 v59, v59, v108, v109
	v_max3_f32 v58, v58, v107, v90
	v_max3_f32 v59, v59, v92, v93
	v_max3_f32 v58, v58, v91, v110
	v_max3_f32 v59, v59, v112, v113
	v_max3_f32 v58, v58, v111, v94
	v_max3_f32 v59, v59, v96, v97
	v_max3_f32 v58, v58, v95, v59
	v_add_f32_e32 v198, v183, v60
	v_cmp_lt_f32_e32 vcc, s41, v58
	s_cmp_lg_u64 vcc, 0
	s_cselect_b64 s[26:27], -1, 0
	s_cbranch_vccnz .Lu2_9

.Lu2_4:
	s_add_i32 s26, s39, 0x2000
	s_cmpk_lg_i32 s39, 0x4000
	s_cselect_b32 s43, s26, 0
	ds_read_b64_tr_b16 v[126:127], v206 offset:40960
	ds_read_b64_tr_b16 v[128:129], v206 offset:41984
	s_waitcnt lgkmcnt(9)
	v_mfma_f32_32x32x16_f16 v[66:81], v[58:61], v[154:157], v[34:49]
	v_add_f32_e32 v224, v98, v102
	v_add_f32_e32 v225, v99, v103
	v_add_f32_e32 v226, v100, v104
	v_add_f32_e32 v227, v101, v105
	v_cvt_pk_f16_f32 v158, v98, v99
	v_cvt_pk_f16_f32 v159, v100, v101
	ds_read_b64_tr_b16 v[122:123], v207 offset:40960
	ds_read_b64_tr_b16 v[124:125], v207 offset:41984
	s_waitcnt lgkmcnt(10)
	v_mfma_f32_32x32x16_f16 v[50:65], v[114:117], v[154:157], v[34:49]
	v_add_f32_e32 v224, v106, v224
	v_add_f32_e32 v225, v107, v225
	v_add_f32_e32 v226, v108, v226
	v_add_f32_e32 v227, v109, v227
	v_cvt_pk_f16_f32 v160, v102, v103
	v_cvt_pk_f16_f32 v161, v104, v105
	ds_read_b64_tr_b16 v[118:119], v206 offset:43008
	ds_read_b64_tr_b16 v[120:121], v206 offset:44032
	s_waitcnt lgkmcnt(11)
	v_mfma_f32_32x32x16_f16 v[66:81], v[182:185], v[146:149], v[66:81]
	v_add_f32_e32 v224, v110, v224
	v_add_f32_e32 v225, v111, v225
	v_add_f32_e32 v226, v112, v226
	v_add_f32_e32 v227, v113, v227
	v_cvt_pk_f16_f32 v150, v106, v107
	v_cvt_pk_f16_f32 v151, v108, v109
	ds_read_b64_tr_b16 v[114:115], v207 offset:43008
	ds_read_b64_tr_b16 v[116:117], v207 offset:44032
	s_waitcnt lgkmcnt(12)
	v_mfma_f32_32x32x16_f16 v[50:65], v[174:177], v[146:149], v[50:65]
	v_add_f32_e32 v224, v82, v224
	v_add_f32_e32 v225, v83, v225
	v_add_f32_e32 v226, v84, v226
	v_add_f32_e32 v227, v85, v227
	v_cvt_pk_f16_f32 v152, v110, v111
	v_cvt_pk_f16_f32 v153, v112, v113
	ds_read_b64_tr_b16 v[106:107], v206 offset:45056
	ds_read_b64_tr_b16 v[108:109], v206 offset:46080
	s_waitcnt lgkmcnt(13)
	v_mfma_f32_32x32x16_f16 v[66:81], v[178:181], v[138:141], v[66:81]
	v_add_f32_e32 v224, v86, v224
	v_add_f32_e32 v225, v87, v225
	v_add_f32_e32 v226, v88, v226
	v_add_f32_e32 v227, v89, v227
	v_cvt_pk_f16_f32 v142, v82, v83
	v_cvt_pk_f16_f32 v143, v84, v85
	ds_read_b64_tr_b16 v[102:103], v207 offset:45056
	ds_read_b64_tr_b16 v[104:105], v207 offset:46080
	s_waitcnt lgkmcnt(14)
	v_mfma_f32_32x32x16_f16 v[50:65], v[166:169], v[138:141], v[50:65]
	v_add_f32_e32 v224, v90, v224
	v_add_f32_e32 v225, v91, v225
	v_add_f32_e32 v226, v92, v226
	v_add_f32_e32 v227, v93, v227
	v_cvt_pk_f16_f32 v144, v86, v87
	v_cvt_pk_f16_f32 v145, v88, v89
	ds_read_b64_tr_b16 v[98:99], v206 offset:47104
	ds_read_b64_tr_b16 v[100:101], v206 offset:48128
	s_waitcnt lgkmcnt(14)
	v_mfma_f32_32x32x16_f16 v[66:81], v[170:173], v[134:137], v[66:81]
	v_add_f32_e32 v224, v94, v224
	v_add_f32_e32 v225, v95, v225
	v_add_f32_e32 v226, v96, v226
	v_add_f32_e32 v227, v97, v227
	v_cvt_pk_f16_f32 v130, v90, v91
	v_cvt_pk_f16_f32 v131, v92, v93
	ds_read_b64_tr_b16 v[86:87], v207 offset:47104
	ds_read_b64_tr_b16 v[88:89], v207 offset:48128
	v_mfma_f32_32x32x16_f16 v[50:65], v[162:165], v[134:137], v[50:65]
	v_add_f32_e32 v224, v224, v225
	v_add_f32_e32 v226, v226, v227
	v_add_f32_e32 v84, v224, v226
	v_cvt_pk_f16_f32 v132, v94, v95
	v_cvt_pk_f16_f32 v133, v96, v97
	s_add_u32 s54, s50, 0x2000
	s_addc_u32 s55, s51, 0
	s_add_i32 s26, s39, s36
	s_mov_b32 m0, s26
	s_nop 0
	global_load_lds_dwordx4 v221, s[54:55]
	v_max_f32_e32 v82, v66, v67
	s_nop 1
	v_max3_f32 v83, v68, v69, v51
	v_max3_f32 v82, v82, v50, v52
	v_max3_f32 v82, v82, v53, v70
	v_max3_f32 v83, v83, v72, v73
	v_max3_f32 v82, v82, v71, v54
	v_max3_f32 v83, v83, v56, v57
	v_max3_f32 v82, v82, v55, v74
	v_max3_f32 v83, v83, v76, v77
	v_max3_f32 v82, v82, v75, v58
	v_max3_f32 v83, v83, v60, v61
	v_max3_f32 v82, v82, v59, v78
	v_max3_f32 v83, v83, v80, v81
	v_max3_f32 v82, v82, v79, v62
	v_max3_f32 v83, v83, v64, v65
	v_max3_f32 v82, v82, v63, v83
	v_add_f32_e32 v183, v198, v84
	s_add_u32 s54, s52, 0x2000
	s_addc_u32 s55, s53, 0
	s_add_i32 s26, s43, s35
	s_mov_b32 m0, s26
	s_nop 0
	global_load_lds_dwordx4 v222, s[54:55]
	v_cmp_lt_f32_e32 vcc, s41, v82
	s_cmp_lg_u64 vcc, 0
	s_cselect_b64 s[26:27], -1, 0
	s_cbranch_vccnz .Lu2_12
